# baseline (speedup 1.0000x reference)
.LBB0_35:
	s_or_b64 exec, exec, s[0:1]
	s_waitcnt vmcnt(14)
	v_mul_u32_u24_e32 v105, 0x880, v227
	s_waitcnt vmcnt(11)
	v_cvt_pk_f16_f32 v3, v150, v151
	v_cvt_pk_f16_f32 v2, v148, v149
	v_lshl_add_u32 v4, v1, 1, v105
	s_waitcnt vmcnt(10)
	v_cvt_pk_f16_f32 v1, v154, v155
	s_waitcnt lgkmcnt(0)
	v_cvt_pk_f16_f32 v0, v152, v153
	s_barrier
	v_lshl_or_b32 v233, v225, 6, v220
	v_mul_u32_u24_e32 v233, 0x110, v233
	v_add_u32_e32 v233, v233, v223
	v_add_u32_e32 v233, 0x10000, v233
	ds_read_b128 v[180:183], v233
	ds_read_b128 v[184:187], v233 offset:32
	ds_read_b128 v[188:191], v233 offset:64
	ds_read_b128 v[192:195], v233 offset:96
	ds_read_b128 v[196:199], v233 offset:128
	ds_read_b128 v[200:203], v233 offset:160
	ds_read_b128 v[204:207], v233 offset:192
	ds_read_b128 v[208:211], v233 offset:224
	ds_write2_b64 v4, v[2:3], v[0:1] offset1:34
	s_waitcnt vmcnt(9)
	v_cvt_pk_f16_f32 v1, v166, v167
	v_cvt_pk_f16_f32 v0, v164, v165
	s_waitcnt vmcnt(8)
	v_cvt_pk_f16_f32 v3, v158, v159
	v_cvt_pk_f16_f32 v2, v156, v157
	ds_write2_b64 v4, v[0:1], v[2:3] offset0:68 offset1:102
	s_waitcnt vmcnt(7)
	v_cvt_pk_f16_f32 v1, v162, v163
	v_cvt_pk_f16_f32 v0, v160, v161
	s_waitcnt vmcnt(6)
	v_cvt_pk_f16_f32 v3, v170, v171
	v_cvt_pk_f16_f32 v2, v168, v169
	ds_write2_b64 v4, v[0:1], v[2:3] offset0:136 offset1:170
	s_waitcnt vmcnt(5)
	v_cvt_pk_f16_f32 v1, v174, v175
	v_cvt_pk_f16_f32 v0, v172, v173
	s_waitcnt vmcnt(4)
	v_cvt_pk_f16_f32 v3, v178, v179
	v_cvt_pk_f16_f32 v2, v176, v177
	ds_write2_b64 v4, v[0:1], v[2:3] offset0:204 offset1:238
	v_lshlrev_b32_e32 v2, 1, v228
	s_waitcnt vmcnt(1)
	v_cvt_pk_f16_f32 v1, v40, v41
	v_cvt_pk_f16_f32 v0, v38, v39
	v_mad_u32_u24 v3, v227, s6, v2
	ds_write_b64 v3, v[0:1] offset:34816
	s_waitcnt vmcnt(0)
	v_cvt_pk_f16_f32 v1, v36, v37
	v_cvt_pk_f16_f32 v0, v34, v35
	v_mad_u32_u24 v2, v229, s6, v2
	ds_write_b64 v2, v[0:1] offset:34816
	v_mov_b32_e32 v97, 0
	v_mov_b32_e32 v0, 0
	v_mov_b32_e32 v4, 0
	v_mov_b32_e32 v96, 0
	s_and_saveexec_b64 s[0:1], vcc
	s_cbranch_execz .LBB0_37
	v_lshl_add_u32 v1, v220, 1, v230
	v_or_b32_e32 v2, 0x21000, v1
	v_add_u32_e32 v1, 0x21040, v1
	ds_read_u16 v1, v1
	ds_read_u16 v2, v2
	v_cvt_f16_f32_e32 v0, v104
	s_waitcnt lgkmcnt(1)
	v_and_b32_e32 v4, 0xffff, v1
	v_pack_b32_f16 v0, v0, 0
	s_waitcnt lgkmcnt(0)
	v_and_b32_e32 v96, 0xffff, v2
.LBB0_37:
	s_or_b64 exec, exec, s[0:1]
	v_mov_b32_e32 v98, v97
	v_mov_b32_e32 v99, v97
	v_mov_b32_e32 v5, v97
	v_mov_b32_e32 v6, v97
	v_mov_b32_e32 v7, v97
	v_mov_b32_e32 v1, v97
	v_mov_b32_e32 v2, v97
	v_mov_b32_e32 v3, v97
	s_mov_b32 s0, 0x10000
	v_or_b32_e32 v8, 0x21000, v223
	v_mfma_f32_32x32x16_f16 v[32:47], v[96:99], v[0:3], 0
	v_mfma_f32_32x32x16_f16 v[16:31], v[4:7], v[0:3], 0
	v_or_b32_e32 v114, 0x21000, v223
	v_cmp_eq_u32_e64 s[0:1], 0, v225
	s_and_b64 vcc, vcc, s[0:1]
	s_waitcnt lgkmcnt(0)
	v_mfma_f32_32x32x16_f16 v[32:47], v[180:183], v[92:95], v[32:47]
	ds_read_b128 v[148:151], v233 offset:8704
	ds_read_b128 v[152:155], v233 offset:8736
	v_mfma_f32_32x32x16_f16 v[32:47], v[184:187], v[88:91], v[32:47]
	ds_read_b128 v[156:159], v233 offset:8768
	ds_read_b128 v[160:163], v233 offset:8800
	v_mfma_f32_32x32x16_f16 v[32:47], v[188:191], v[84:87], v[32:47]
	ds_read_b128 v[164:167], v233 offset:8832
	ds_read_b128 v[168:171], v233 offset:8864
	v_mfma_f32_32x32x16_f16 v[32:47], v[192:195], v[80:83], v[32:47]
	ds_read_b128 v[172:175], v233 offset:8896
	ds_read_b128 v[176:179], v233 offset:8928
	v_mfma_f32_32x32x16_f16 v[32:47], v[196:199], v[76:79], v[32:47]
	ds_read_b128 v[8:11], v114
	ds_read_b128 v[12:15], v114 offset:32
	v_mfma_f32_32x32x16_f16 v[32:47], v[200:203], v[72:75], v[32:47]
	ds_read_b128 v[234:237], v114 offset:64
	ds_read_b128 v[238:241], v114 offset:96
	v_mfma_f32_32x32x16_f16 v[32:47], v[204:207], v[68:71], v[32:47]
	ds_read_b128 v[242:245], v114 offset:128
	ds_read_b128 v[106:109], v114 offset:160
	v_mfma_f32_32x32x16_f16 v[32:47], v[208:211], v[64:67], v[32:47]
	ds_read_b128 v[110:113], v114 offset:192
	ds_read_b128 v[0:3], v114 offset:224
	s_waitcnt lgkmcnt(0)
	v_dot2c_f32_f16_e32 v98, v92, v8
	v_mfma_f32_32x32x16_f16 v[16:31], v[148:151], v[92:95], v[16:31]
	v_dot2c_f32_f16_e32 v98, v93, v9
	v_dot2c_f32_f16_e32 v98, v94, v10
	v_dot2c_f32_f16_e32 v98, v95, v11
	v_dot2c_f32_f16_e32 v98, v88, v12
	v_mfma_f32_32x32x16_f16 v[16:31], v[152:155], v[88:91], v[16:31]
	v_dot2c_f32_f16_e32 v98, v89, v13
	v_dot2c_f32_f16_e32 v98, v90, v14
	v_dot2c_f32_f16_e32 v98, v91, v15
	v_dot2c_f32_f16_e32 v98, v84, v234
	v_mfma_f32_32x32x16_f16 v[16:31], v[156:159], v[84:87], v[16:31]
	v_dot2c_f32_f16_e32 v98, v85, v235
	v_dot2c_f32_f16_e32 v98, v86, v236
	v_dot2c_f32_f16_e32 v98, v87, v237
	v_dot2c_f32_f16_e32 v98, v80, v238
	v_mfma_f32_32x32x16_f16 v[16:31], v[160:163], v[80:83], v[16:31]
	v_dot2c_f32_f16_e32 v98, v81, v239
	v_dot2c_f32_f16_e32 v98, v82, v240
	v_dot2c_f32_f16_e32 v98, v83, v241
	v_dot2c_f32_f16_e32 v98, v76, v242
	v_mfma_f32_32x32x16_f16 v[16:31], v[164:167], v[76:79], v[16:31]
	v_dot2c_f32_f16_e32 v98, v77, v243
	v_dot2c_f32_f16_e32 v98, v78, v244
	v_dot2c_f32_f16_e32 v98, v79, v245
	v_dot2c_f32_f16_e32 v98, v72, v106
	v_mfma_f32_32x32x16_f16 v[16:31], v[168:171], v[72:75], v[16:31]
	v_dot2c_f32_f16_e32 v98, v73, v107
	v_dot2c_f32_f16_e32 v98, v74, v108
	v_dot2c_f32_f16_e32 v98, v75, v109
	v_dot2c_f32_f16_e32 v98, v68, v110
	v_mfma_f32_32x32x16_f16 v[16:31], v[172:175], v[68:71], v[16:31]
	v_dot2c_f32_f16_e32 v98, v69, v111
	v_dot2c_f32_f16_e32 v98, v70, v112
	v_dot2c_f32_f16_e32 v98, v71, v113
	v_cvt_pk_f16_f32 v7, v38, v39
	v_cvt_pk_f16_f32 v6, v36, v37
	v_cvt_pk_f16_f32 v5, v34, v35
	v_cvt_pk_f16_f32 v4, v32, v33
	v_dot2c_f32_f16_e32 v98, v64, v0
	v_dot2c_f32_f16_e32 v98, v65, v1
	v_dot2c_f32_f16_e32 v98, v66, v2
	v_mfma_f32_32x32x16_f16 v[16:31], v[176:179], v[64:67], v[16:31]
	v_dot2c_f32_f16_e32 v98, v67, v3
	v_cvt_pk_f16_f32 v35, v46, v47
	v_cvt_pk_f16_f32 v34, v44, v45
	v_cvt_pk_f16_f32 v33, v42, v43
	v_cvt_pk_f16_f32 v32, v40, v41
	ds_bpermute_b32 v36, v102, v98
	v_cvt_f32_i32_e32 v37, v226
	v_mfma_f32_32x32x16_f16 v[0:15], v[4:7], v[60:63], 0
	s_nop 3
	v_cvt_pk_f16_f32 v23, v22, v23
	v_cvt_pk_f16_f32 v22, v20, v21
	v_cvt_pk_f16_f32 v21, v18, v19
	v_cvt_pk_f16_f32 v20, v16, v17
	v_cvt_pk_f16_f32 v19, v30, v31
	v_cvt_pk_f16_f32 v18, v28, v29
	v_cvt_pk_f16_f32 v17, v26, v27
	v_mfma_f32_32x32x16_f16 v[0:15], v[32:35], v[56:59], v[0:15]
	v_cvt_pk_f16_f32 v16, v24, v25
	s_waitcnt lgkmcnt(0)
	v_add_f32_e32 v36, v98, v36
	v_cvt_f16_f32_e32 v26, v100
	v_mov_b32_e32 v98, v97
	v_lshlrev_b32_e32 v32, 4, v218
	v_mfma_f32_32x32x16_f16 v[0:15], v[20:23], v[52:55], v[0:15]
	v_fma_mixlo_f16 v20, v37, v104, v36
	v_pack_b32_f16 v20, v20, 0
	v_pack_b32_f16 v21, v26, 0
	v_cndmask_b32_e32 v96, 0, v21, vcc
	v_mfma_f32_32x32x16_f16 v[0:15], v[16:19], v[48:51], v[0:15]
	v_cndmask_b32_e32 v16, 0, v20, vcc
	v_mov_b32_e32 v17, v97
	v_mov_b32_e32 v18, v97
	v_mov_b32_e32 v19, v97
	v_cmp_ne_u32_e32 vcc, 0, v225
	s_nop 0
	v_mfma_f32_32x32x16_f16 v[0:15], v[16:19], v[96:99], v[0:15]
	v_lshlrev_b32_e32 v70, 2, v215
	v_lshl_add_u32 v70, v214, 4, v70
	global_load_dwordx4 v[16:19], v70, s[64:65]
	global_load_dwordx4 v[20:23], v70, s[64:65] offset:32
	global_load_dwordx4 v[24:27], v70, s[64:65] offset:64
	global_load_dwordx4 v[28:31], v70, s[64:65] offset:96
	s_and_saveexec_b64 s[6:7], vcc
	s_cbranch_execz .LBB0_39
	v_lshl_or_b32 v71, v251, 12, v32
	v_add_u32_e32 v71, 0x18800, v71
	s_nop 7
	ds_write_b128 v71, v[0:3]
	ds_write_b128 v71, v[4:7] offset:1024
	ds_write_b128 v71, v[8:11] offset:2048
	ds_write_b128 v71, v[12:15] offset:3072
